# GEMM phase prologues: both stage-load groups issued before the first wait+barrier (vmcnt(2)->vmcnt(8) moved below the second group), on top of v102
# baseline (speedup 1.0000x reference)
.LBB0_416:
	s_add_u32 s8, s0, 0x1fc00000
	s_addc_u32 s9, s1, 0
	s_add_i32 s20, s12, 0x18000
	s_mov_b32 s6, s62
	s_mov_b32 s7, s63
	s_mov_b32 m0, s20
	v_readlane_b32 s0, v251, 39
	s_add_i32 s21, s12, 0x1a000
	s_add_i32 s22, s12, 0x8000
	s_add_i32 s23, s12, 0xa000
	s_nop 0
	s_nop 0
	buffer_load_dwordx4 v130, s[4:7], s0 offen lds
	s_mov_b32 m0, s21
	v_readlane_b32 s0, v251, 40
	s_add_i32 s24, s12, 0x1c000
	s_add_i32 s25, s12, 0x1e000
	v_and_b32_e32 v1, 15, v0
	v_and_b32_e32 v2, 48, v0
	v_lshlrev_b32_e32 v0, 2, v0
	buffer_load_dwordx4 v130, s[4:7], s0 offen lds
	s_mov_b32 m0, s22
	v_readlane_b32 s0, v251, 41
	v_lshl_or_b32 v1, v1, 6, v2
	v_and_b32_e32 v0, 32, v0
	s_lshl_b32 s26, s27, 6
	s_add_i32 s28, s12, 0xe000
	s_mov_b32 s29, 0
	buffer_load_dwordx4 v129, s[60:63], s0 offen lds
	s_mov_b32 m0, s23
	v_readlane_b32 s0, v251, 43
	v_readlane_b32 s38, v251, 31
	v_readlane_b32 s37, v251, 32
	v_readlane_b32 s42, v251, 45
	v_readlane_b32 s41, v251, 42
	s_nop 0
	buffer_load_dwordx4 v129, s[60:63], s0 offen lds
	s_mov_b32 m0, s24
	v_readlane_b32 s0, v251, 44
	s_nop 4
	buffer_load_dwordx4 v130, s[4:7], s0 offen lds
	s_mov_b32 m0, s25
	v_readlane_b32 s0, v251, 46
	s_nop 4
	buffer_load_dwordx4 v130, s[4:7], s0 offen lds
	s_lshl_b32 s0, s27, 13
	v_bitop3_b32 v2, v1, s0, v0 bitop3:0xde
	s_lshl_b32 s0, s11, 5
	s_and_b32 s0, s0, 0x60
	s_lshl_b32 s1, s0, 7
	v_bitop3_b32 v0, s1, v1, v0 bitop3:0xf6
	s_waitcnt vmcnt(8)
	s_barrier
	s_waitcnt vmcnt(6)
	s_add_i32 s27, s12, 0xc000
	v_or_b32_e32 v0, 0x10000, v0
	s_cmpk_lt_u32 s10, 0x100
	s_cselect_b64 s[10:11], -1, 0
	v_add_u32_e32 v132, 0, v0
	v_add_u32_e32 v133, 0, v2
	s_lshl_b32 s64, s0, 1
	s_barrier
	s_branch .LBB0_419

.LBB0_636:
	s_add_i32 s26, s16, 0x18000
	s_add_i32 s7, s21, 0x80
	s_mov_b32 m0, s26
	s_add_i32 s27, s16, 0x1a000
	buffer_load_dwordx4 v141, s[60:63], s7 offen lds
	s_add_i32 s7, s21, 0x8080
	s_mov_b32 m0, s27
	v_and_b32_e32 v1, 15, v0
	v_and_b32_e32 v2, 48, v0
	v_lshlrev_b32_e32 v0, 2, v0
	buffer_load_dwordx4 v141, s[60:63], s7 offen lds
	v_lshl_or_b32 v2, v1, 6, v2
	v_and_b32_e32 v3, 32, v0
	ds_read_b64 v[0:1], v140
	s_lshl_b32 s0, s0, 5
	s_lshl_b32 s25, s1, 6
	s_lshl_b32 s1, s1, 13
	s_and_b32 s0, s0, 0x60
	v_bitop3_b32 v4, v2, s1, v3 bitop3:0xde
	s_lshl_b32 s1, s0, 7
	s_add_i32 s28, s16, 0x8000
	v_bitop3_b32 v2, s1, v2, v3 bitop3:0xf6
	s_mov_b32 m0, s28
	s_movk_i32 s1, 0x80
	s_add_i32 s29, s16, 0xa000
	s_waitcnt lgkmcnt(0)
	buffer_load_dwordx4 v0, s[60:63], s1 offen lds
	s_mov_b32 m0, s29
	s_add_i32 s30, s16, 0x1c000
	buffer_load_dwordx4 v1, s[60:63], s1 offen lds
	s_add_i32 s1, s21, 0x10080
	s_mov_b32 m0, s30
	s_add_i32 s31, s16, 0x1e000
	buffer_load_dwordx4 v141, s[60:63], s1 offen lds
	s_add_i32 s1, s21, 0x18080
	s_mov_b32 m0, s31
	s_add_i32 s34, s16, 0xc000
	buffer_load_dwordx4 v141, s[60:63], s1 offen lds
	s_add_i32 s35, s16, 0xe000
	s_waitcnt vmcnt(8)
	s_barrier
	s_waitcnt vmcnt(6)
	s_cmpk_lt_u32 s6, 0x100
	v_or_b32_e32 v2, 0x10000, v2
	s_cselect_b64 s[6:7], -1, 0
	s_lshl_b32 s1, s59, 19
	s_or_b32 s36, s1, 0x1e00000
	s_or_b32 s37, s38, 0x1c00000
	s_bitset1_b32 s38, 25
	s_mov_b32 s39, 0
	v_add_u32_e32 v142, 0, v2
	v_add_u32_e32 v143, 0, v4
	s_lshl_b32 s64, s0, 1
	v_readlane_b32 s40, v251, 11
	v_readlane_b32 s41, v252, 18
	v_mov_b32_e32 v0, v134
	v_mov_b32_e32 v1, v134
	v_mov_b32_e32 v2, v134
	v_mov_b32_e32 v3, v134
	v_mov_b32_e32 v4, v134
	v_mov_b32_e32 v5, v134
	v_mov_b32_e32 v6, v134
	v_mov_b32_e32 v7, v134
	v_mov_b32_e32 v8, v134
	v_mov_b32_e32 v9, v134
	v_mov_b32_e32 v10, v134
	v_mov_b32_e32 v11, v134
	v_mov_b32_e32 v12, v134
	v_mov_b32_e32 v13, v134
	v_mov_b32_e32 v14, v134
	v_mov_b32_e32 v15, v134
	s_waitcnt vmcnt(19)
	v_mov_b32_e32 v16, v134
	v_mov_b32_e32 v17, v134
	v_mov_b32_e32 v18, v134
	v_mov_b32_e32 v19, v134
	s_waitcnt vmcnt(18)
	v_mov_b32_e32 v20, v134
	v_mov_b32_e32 v21, v134
	v_mov_b32_e32 v22, v134
	v_mov_b32_e32 v23, v134
	s_waitcnt vmcnt(17)
	v_mov_b32_e32 v24, v134
	v_mov_b32_e32 v25, v134
	v_mov_b32_e32 v26, v134
	v_mov_b32_e32 v27, v134
	s_waitcnt vmcnt(16)
	v_mov_b32_e32 v28, v134
	v_mov_b32_e32 v29, v134
	v_mov_b32_e32 v30, v134
	v_mov_b32_e32 v31, v134
	s_waitcnt vmcnt(15)
	v_mov_b32_e32 v32, v134
	v_mov_b32_e32 v33, v134
	v_mov_b32_e32 v34, v134
	v_mov_b32_e32 v35, v134
	v_mov_b32_e32 v36, v134
	v_mov_b32_e32 v37, v134
	v_mov_b32_e32 v38, v134
	v_mov_b32_e32 v39, v134
	v_mov_b32_e32 v40, v134
	v_mov_b32_e32 v41, v134
	v_mov_b32_e32 v42, v134
	v_mov_b32_e32 v43, v134
	v_mov_b32_e32 v44, v134
	v_mov_b32_e32 v45, v134
	v_mov_b32_e32 v46, v134
	v_mov_b32_e32 v47, v134
	v_mov_b32_e32 v48, v134
	v_mov_b32_e32 v49, v134
	v_mov_b32_e32 v50, v134
	v_mov_b32_e32 v51, v134
	v_mov_b32_e32 v52, v134
	v_mov_b32_e32 v53, v134
	v_mov_b32_e32 v54, v134
	v_mov_b32_e32 v55, v134
	s_waitcnt vmcnt(14)
	v_mov_b64_e32 v[56:57], 0
	v_mov_b64_e32 v[58:59], 0
	v_mov_b64_e32 v[60:61], 0
	v_mov_b64_e32 v[62:63], 0
	v_mov_b64_e32 v[64:65], 0
	v_mov_b64_e32 v[66:67], 0
	v_mov_b64_e32 v[68:69], 0
	v_mov_b64_e32 v[70:71], 0
	v_mov_b64_e32 v[72:73], 0
	v_mov_b64_e32 v[74:75], 0
	v_mov_b64_e32 v[76:77], 0
	v_mov_b64_e32 v[78:79], 0
	v_mov_b64_e32 v[80:81], 0
	v_mov_b64_e32 v[82:83], 0
	v_mov_b64_e32 v[84:85], 0
	v_mov_b64_e32 v[86:87], 0
	v_mov_b64_e32 v[88:89], 0
	v_mov_b64_e32 v[90:91], 0
	v_mov_b64_e32 v[92:93], 0
	v_mov_b64_e32 v[94:95], 0
	v_mov_b64_e32 v[96:97], 0
	v_mov_b64_e32 v[98:99], 0
	v_mov_b64_e32 v[100:101], 0
	v_mov_b64_e32 v[102:103], 0
	v_mov_b64_e32 v[104:105], 0
	v_mov_b64_e32 v[106:107], 0
	v_mov_b64_e32 v[108:109], 0
	v_mov_b64_e32 v[110:111], 0
	v_mov_b64_e32 v[112:113], 0
	v_mov_b64_e32 v[114:115], 0
	v_mov_b64_e32 v[116:117], 0
	v_mov_b64_e32 v[118:119], 0
	v_mov_b64_e32 v[120:121], 0
	v_mov_b64_e32 v[122:123], 0
	v_mov_b64_e32 v[124:125], 0
	v_mov_b64_e32 v[126:127], 0
	s_barrier
	s_branch .LBB0_639

.LBB0_1151:
	s_add_u32 s36, s14, 0x102000
	s_mul_i32 s64, s59, 0x1800
	s_addc_u32 s37, s15, 0
	s_lshl_b64 s[10:11], s[64:65], 2
	s_waitcnt lgkmcnt(0)
	s_add_u32 s0, s0, s10
	s_addc_u32 s1, s1, s11
	s_add_u32 s20, s0, 0x2000
	s_addc_u32 s21, s1, 0
	s_add_i32 s38, s25, 0x18000
	s_mov_b32 s10, s6
	s_mov_b32 s11, s7
	s_mov_b32 m0, s38
	v_readlane_b32 s0, v251, 55
	s_add_i32 s39, s25, 0x1a000
	s_add_i32 s40, s25, 0x8000
	s_add_i32 s41, s25, 0xa000
	s_nop 0
	s_nop 0
	buffer_load_dwordx4 v149, s[8:11], s0 offen lds
	s_mov_b32 m0, s39
	v_readlane_b32 s0, v251, 56
	s_add_i32 s42, s25, 0x1c000
	s_add_i32 s43, s25, 0x1e000
	v_and_b32_e32 v0, 15, v148
	v_and_b32_e32 v1, 48, v148
	v_lshl_or_b32 v0, v0, 6, v1
	buffer_load_dwordx4 v149, s[8:11], s0 offen lds
	s_mov_b32 m0, s40
	v_readlane_b32 s0, v251, 57
	v_and_b32_e32 v1, 32, v208
	s_lshl_b32 s44, s45, 6
	s_add_i32 s46, s25, 0xc000
	s_add_i32 s47, s25, 0xe000
	s_mov_b32 s48, 0
	buffer_load_dwordx4 v149, s[4:7], s0 offen lds
	s_mov_b32 m0, s41
	v_readlane_b32 s0, v251, 59
	v_readlane_b32 s54, v251, 48
	v_readlane_b32 s55, v252, 21
	v_readlane_b32 s59, v251, 61
	v_readlane_b32 s58, v251, 58
	s_nop 0
	buffer_load_dwordx4 v149, s[4:7], s0 offen lds
	s_mov_b32 m0, s42
	v_readlane_b32 s0, v251, 60
	s_nop 4
	buffer_load_dwordx4 v149, s[8:11], s0 offen lds
	s_mov_b32 m0, s43
	v_readlane_b32 s0, v251, 62
	s_nop 4
	buffer_load_dwordx4 v149, s[8:11], s0 offen lds
	s_lshl_b32 s0, s45, 13
	v_bitop3_b32 v2, v0, s0, v1 bitop3:0xde
	s_lshl_b32 s0, s23, 5
	s_and_b32 s45, s0, 0x60
	s_lshl_b32 s0, s45, 7
	v_bitop3_b32 v0, s0, v0, v1 bitop3:0xf6
	s_waitcnt vmcnt(8)
	s_barrier
	s_waitcnt vmcnt(6)
	v_or_b32_e32 v0, 0x10000, v0
	s_cmpk_lt_u32 s22, 0x100
	s_cselect_b64 s[22:23], -1, 0
	v_add_u32_e32 v151, 0, v0
	v_add_u32_e32 v152, 0, v2
	s_barrier
	s_branch .LBB0_1154

.LBB0_1173:
	s_cmp_eq_u32 s59, 0
	s_cselect_b64 s[20:21], -1, 0
	s_add_i32 s48, s40, 0x18000
	s_mov_b32 s10, s6
	s_mov_b32 s11, s7
	s_mov_b32 m0, s48
	v_readlane_b32 s3, v251, 55
	s_add_i32 s49, s40, 0x1a000
	s_add_i32 s50, s40, 0x8000
	s_add_i32 s51, s40, 0xa000
	s_nop 0
	s_nop 0
	buffer_load_dwordx4 v244, s[8:11], s3 offen lds
	s_mov_b32 m0, s49
	v_readlane_b32 s3, v251, 56
	s_add_i32 s52, s40, 0x1c000
	s_add_i32 s53, s40, 0x1e000
	v_and_b32_e32 v0, 15, v148
	v_and_b32_e32 v1, 48, v148
	s_and_b32 s1, s1, 3
	buffer_load_dwordx4 v244, s[8:11], s3 offen lds
	s_mov_b32 m0, s50
	v_readlane_b32 s3, v251, 57
	v_lshl_or_b32 v0, v0, 6, v1
	v_and_b32_e32 v1, 32, v208
	s_lshl_b32 s55, s2, 6
	s_lshl_b32 s56, s1, 5
	s_add_i32 s57, s40, 0xc000
	buffer_load_dwordx4 v244, s[4:7], s3 offen lds
	s_mov_b32 m0, s51
	v_readlane_b32 s3, v251, 59
	s_add_i32 s58, s40, 0xe000
	s_mov_b32 s54, 0
	v_readlane_b32 s60, v251, 48
	v_readlane_b32 s77, v252, 21
	v_readlane_b32 s76, v252, 20
	buffer_load_dwordx4 v244, s[4:7], s3 offen lds
	s_mov_b32 m0, s52
	v_readlane_b32 s3, v251, 60
	s_nop 4
	buffer_load_dwordx4 v244, s[8:11], s3 offen lds
	s_mov_b32 m0, s53
	v_readlane_b32 s3, v251, 62
	s_nop 4
	buffer_load_dwordx4 v244, s[8:11], s3 offen lds
	s_lshl_b32 s3, s2, 13
	v_bitop3_b32 v2, v0, s3, v1 bitop3:0xde
	s_lshl_b32 s3, s1, 12
	s_cmpk_lt_u32 s0, 0x100
	s_cselect_b64 s[22:23], -1, 0
	s_lshl_b32 s0, s2, 2
	s_or_b32 s0, s0, s1
	v_bitop3_b32 v0, s3, v0, v1 bitop3:0xf6
	s_mov_b32 s10, s59
	s_lshl_b32 s59, s0, 6
	s_lshl_b32 s3, s1, 10
	s_cmp_eq_u32 s0, 0
	s_cselect_b64 s[24:25], -1, 0
	s_lshl_b32 s2, s2, 8
	s_waitcnt vmcnt(8)
	s_barrier
	s_waitcnt vmcnt(6)
	s_add_i32 s2, s2, 0
	v_or_b32_e32 v0, 0x10000, v0
	s_mul_i32 s64, s10, 0x1800
	s_lshl_b32 s0, s10, 10
	s_mov_b32 s1, s65
	s_add_i32 s67, s2, s3
	s_lshl_b32 s66, s10, 18
	s_add_i32 s67, s67, 0x21000
	v_add_u32_e32 v208, 0, v0
	v_add_u32_e32 v246, 0, v2
	s_lshl_b64 s[26:27], s[64:65], 2
	s_lshl_b64 s[28:29], s[0:1], 2
	v_readlane_b32 s10, v251, 61
	v_readlane_b32 s11, v251, 58
	s_barrier
	s_branch .LBB0_1176

.LBB0_1412:
	s_add_u32 s8, s18, 0x1fc00000
	s_addc_u32 s6, s19, 0
	s_add_u32 s12, s18, 0x1b400000
	v_and_b32_e32 v1, 15, v196
	v_and_b32_e32 v2, 48, v196
	s_addc_u32 s7, s19, 0
	s_lshl_b32 s9, s4, 6
	v_lshl_or_b32 v1, v1, 6, v2
	v_lshlrev_b32_e32 v2, 2, v196
	s_and_b32 s5, s5, 3
	v_writelane_b32 v253, s9, 61
	s_lshl_b32 s9, s4, 13
	v_and_b32_e32 v2, 32, v2
	v_bitop3_b32 v3, v1, s9, v2 bitop3:0xde
	s_lshl_b32 s9, s5, 5
	v_writelane_b32 v253, s9, 63
	s_lshl_b32 s9, s5, 12
	s_add_i32 s83, s73, 0x18000
	v_bitop3_b32 v1, s9, v1, v2 bitop3:0xf6
	s_add_i32 s9, s66, 0x80
	s_mov_b32 m0, s83
	s_add_i32 s84, s73, 0x1a000
	buffer_load_dwordx4 v194, s[60:63], s9 offen lds
	s_add_i32 s9, s9, s2
	s_mov_b32 m0, s84
	s_add_i32 s85, s73, 0x8000
	buffer_load_dwordx4 v194, s[60:63], s9 offen lds
	s_add_i32 s9, s57, 0x80
	s_mov_b32 m0, s85
	s_add_i32 s86, s73, 0xa000
	buffer_load_dwordx4 v192, s[60:63], s9 offen lds
	s_add_i32 s9, s9, s2
	s_mov_b32 m0, s86
	s_add_i32 s87, s73, 0x1c000
	buffer_load_dwordx4 v192, s[60:63], s9 offen lds
	s_addk_i32 s3, 0x80
	s_mov_b32 m0, s87
	s_add_i32 s90, s73, 0x1e000
	buffer_load_dwordx4 v194, s[60:63], s3 offen lds
	s_add_i32 s3, s3, s2
	s_mov_b32 m0, s90
	s_cmp_lt_u32 s10, 64
	buffer_load_dwordx4 v194, s[60:63], s3 offen lds
	s_cselect_b64 s[24:25], -1, 0
	s_add_i32 s91, s73, 0xc000
	s_add_i32 s92, s73, 0xe000
	s_cmpk_lt_u32 s10, 0x100
	s_cselect_b64 s[26:27], -1, 0
	s_and_b32 s13, s7, 0xffff
	s_lshl_b32 s5, s5, 6
	s_lshl_b32 s94, s4, 17
	s_and_b32 s9, s6, 0xffff
	s_cmp_lt_i32 s95, s1
	v_writelane_b32 v253, s5, 56
	s_cselect_b64 s[4:5], -1, 0
	v_cmp_eq_u32_e64 s[2:3], 0, v0
	v_cndmask_b32_e64 v0, 0, 1, s[4:5]
	s_cmp_lt_i32 s95, s0
	v_readfirstlane_b32 s4, v0
	s_waitcnt vmcnt(8)
	s_barrier
	s_waitcnt vmcnt(6)
	v_or_b32_e32 v1, 0x10000, v1
	s_mov_b32 s10, -1
	v_writelane_b32 v254, s4, 5
	s_cselect_b32 s4, 0, 3
	s_sub_i32 s5, s93, s0
	s_sub_i32 s0, s95, s0
	v_writelane_b32 v254, s4, 7
	s_mul_i32 s4, s51, s93
	s_add_i32 s0, s0, s1
	v_writelane_b32 v254, s5, 11
	s_add_i32 s0, s0, s4
	v_writelane_b32 v254, s0, 13
	s_add_i32 s0, s4, s95
	s_mov_b32 s36, 0
	s_mov_b32 s11, s63
	v_writelane_b32 v254, s0, 9
	v_add_u32_e32 v199, 0, v1
	v_add_u32_e32 v200, 0, v3
	s_mov_b32 s64, s10
	v_mov_b64_e32 v[64:65], 0
	v_mov_b64_e32 v[66:67], 0
	v_mov_b64_e32 v[68:69], 0
	v_mov_b64_e32 v[70:71], 0
	v_mov_b64_e32 v[72:73], 0
	v_mov_b64_e32 v[74:75], 0
	v_mov_b64_e32 v[76:77], 0
	v_mov_b64_e32 v[78:79], 0
	v_mov_b64_e32 v[80:81], 0
	v_mov_b64_e32 v[82:83], 0
	v_mov_b64_e32 v[84:85], 0
	v_mov_b64_e32 v[86:87], 0
	v_mov_b64_e32 v[88:89], 0
	v_mov_b64_e32 v[90:91], 0
	v_mov_b64_e32 v[92:93], 0
	v_mov_b64_e32 v[94:95], 0
	v_mov_b64_e32 v[96:97], 0
	v_mov_b64_e32 v[98:99], 0
	v_mov_b64_e32 v[100:101], 0
	v_mov_b64_e32 v[102:103], 0
	v_mov_b64_e32 v[104:105], 0
	v_mov_b64_e32 v[106:107], 0
	v_mov_b64_e32 v[108:109], 0
	v_mov_b64_e32 v[110:111], 0
	v_mov_b64_e32 v[112:113], 0
	v_mov_b64_e32 v[114:115], 0
	v_mov_b64_e32 v[116:117], 0
	v_mov_b64_e32 v[118:119], 0
	v_mov_b64_e32 v[120:121], 0
	v_mov_b64_e32 v[122:123], 0
	v_mov_b64_e32 v[124:125], 0
	v_mov_b64_e32 v[126:127], 0
	v_mov_b64_e32 v[128:129], 0
	v_mov_b64_e32 v[130:131], 0
	v_mov_b64_e32 v[132:133], 0
	v_mov_b64_e32 v[134:135], 0
	v_mov_b64_e32 v[136:137], 0
	v_mov_b64_e32 v[138:139], 0
	v_mov_b64_e32 v[140:141], 0
	v_mov_b64_e32 v[142:143], 0
	v_mov_b64_e32 v[144:145], 0
	v_mov_b64_e32 v[146:147], 0
	v_mov_b64_e32 v[148:149], 0
	v_mov_b64_e32 v[150:151], 0
	v_mov_b64_e32 v[152:153], 0
	v_mov_b64_e32 v[154:155], 0
	v_mov_b64_e32 v[156:157], 0
	v_mov_b64_e32 v[158:159], 0
	v_mov_b64_e32 v[160:161], 0
	v_mov_b64_e32 v[162:163], 0
	v_mov_b64_e32 v[164:165], 0
	v_mov_b64_e32 v[166:167], 0
	v_mov_b64_e32 v[168:169], 0
	v_mov_b64_e32 v[170:171], 0
	v_mov_b64_e32 v[172:173], 0
	v_mov_b64_e32 v[174:175], 0
	v_mov_b64_e32 v[176:177], 0
	v_mov_b64_e32 v[178:179], 0
	v_mov_b64_e32 v[180:181], 0
	v_mov_b64_e32 v[182:183], 0
	v_mov_b64_e32 v[184:185], 0
	v_mov_b64_e32 v[186:187], 0
	v_mov_b64_e32 v[188:189], 0
	v_mov_b64_e32 v[190:191], 0
	s_barrier
	s_branch .LBB0_1415

.LBB0_1564:
	s_add_u32 s8, s0, 0x1fc00000
	s_addc_u32 s0, s1, 0
	s_add_i32 s22, s14, 0x18000
	s_mov_b32 s6, s62
	s_mov_b32 s7, s63
	s_mov_b32 m0, s22
	v_readlane_b32 s1, v252, 6
	s_add_i32 s23, s14, 0x1a000
	s_add_i32 s24, s14, 0x8000
	s_add_i32 s25, s14, 0xa000
	s_nop 0
	s_nop 0
	buffer_load_dwordx4 v130, s[4:7], s1 offen lds
	s_mov_b32 m0, s23
	v_readlane_b32 s1, v252, 7
	s_add_i32 s26, s14, 0x1c000
	s_add_i32 s27, s14, 0x1e000
	v_and_b32_e32 v1, 15, v0
	v_and_b32_e32 v2, 48, v0
	v_lshlrev_b32_e32 v0, 2, v0
	buffer_load_dwordx4 v130, s[4:7], s1 offen lds
	s_mov_b32 m0, s24
	v_readlane_b32 s1, v252, 8
	v_lshl_or_b32 v1, v1, 6, v2
	v_and_b32_e32 v0, 32, v0
	s_lshl_b32 s28, s11, 6
	s_add_i32 s30, s14, 0xc000
	s_add_i32 s31, s14, 0xe000
	buffer_load_dwordx4 v129, s[60:63], s1 offen lds
	s_mov_b32 m0, s25
	v_readlane_b32 s1, v252, 10
	s_mov_b32 s34, 0
	v_readlane_b32 s43, v252, 12
	v_readlane_b32 s42, v252, 9
	s_nop 1
	buffer_load_dwordx4 v129, s[60:63], s1 offen lds
	s_mov_b32 m0, s26
	v_readlane_b32 s1, v252, 11
	s_nop 4
	buffer_load_dwordx4 v130, s[4:7], s1 offen lds
	s_mov_b32 m0, s27
	v_readlane_b32 s1, v252, 13
	s_nop 4
	buffer_load_dwordx4 v130, s[4:7], s1 offen lds
	s_lshl_b32 s1, s11, 13
	v_bitop3_b32 v2, v1, s1, v0 bitop3:0xde
	s_lshl_b32 s1, s10, 5
	s_and_b32 s29, s1, 0x60
	s_lshl_b32 s1, s29, 7
	v_bitop3_b32 v0, s1, v1, v0 bitop3:0xf6
	s_waitcnt vmcnt(8)
	s_barrier
	s_waitcnt vmcnt(6)
	v_or_b32_e32 v0, 0x10000, v0
	s_cmpk_lt_u32 s9, 0x100
	s_cselect_b64 s[12:13], -1, 0
	s_and_b32 s9, s0, 0xffff
	v_add_u32_e32 v132, 0, v0
	v_add_u32_e32 v133, 0, v2
	v_readlane_b32 s10, v251, 47
	v_readlane_b32 s11, v251, 63
	s_barrier
	s_branch .LBB0_1567

.LBB0_1636:
	s_add_i32 s51, s42, 0x18000
	s_mov_b32 s10, s6
	s_mov_b32 s11, s7
	s_mov_b32 m0, s51
	v_readlane_b32 s3, v252, 28
	s_add_i32 s52, s42, 0x1a000
	s_add_i32 s53, s42, 0x8000
	s_add_i32 s54, s42, 0xa000
	s_nop 0
	s_nop 0
	buffer_load_dwordx4 v243, s[8:11], s3 offen lds
	s_mov_b32 m0, s52
	v_readlane_b32 s3, v252, 29
	s_add_i32 s55, s42, 0x1c000
	s_add_i32 s56, s42, 0x1e000
	v_and_b32_e32 v1, 15, v0
	v_and_b32_e32 v2, 48, v0
	v_lshlrev_b32_e32 v0, 2, v0
	buffer_load_dwordx4 v243, s[8:11], s3 offen lds
	s_mov_b32 m0, s53
	v_readlane_b32 s3, v252, 30
	s_and_b32 s1, s1, 3
	v_lshl_or_b32 v1, v1, 6, v2
	v_and_b32_e32 v0, 32, v0
	s_lshl_b32 s57, s2, 6
	s_lshl_b32 s58, s1, 5
	buffer_load_dwordx4 v243, s[4:7], s3 offen lds
	s_mov_b32 m0, s54
	v_readlane_b32 s3, v252, 32
	s_add_i32 s66, s42, 0xe000
	s_mov_b32 s13, s65
	s_mov_b32 s72, 0
	v_readlane_b32 s40, v251, 48
	v_readlane_b32 s80, v252, 21
	buffer_load_dwordx4 v243, s[4:7], s3 offen lds
	s_mov_b32 m0, s55
	v_readlane_b32 s3, v252, 33
	v_readlane_b32 s79, v252, 20
	s_nop 3
	buffer_load_dwordx4 v243, s[8:11], s3 offen lds
	s_mov_b32 m0, s56
	v_readlane_b32 s3, v252, 35
	s_nop 4
	buffer_load_dwordx4 v243, s[8:11], s3 offen lds
	s_lshl_b32 s10, s2, 13
	v_bitop3_b32 v2, v1, s10, v0 bitop3:0xde
	s_lshl_b32 s10, s1, 12
	s_or_b32 s3, s59, 1
	v_bitop3_b32 v0, s10, v1, v0 bitop3:0xf6
	s_mov_b32 s10, s59
	s_add_i32 s59, s42, 0xc000
	s_cmpk_lt_u32 s0, 0x100
	s_cselect_b64 s[22:23], -1, 0
	s_lshl_b32 s0, s2, 2
	s_or_b32 s0, s0, s1
	s_lshl_b32 s67, s0, 6
	s_lshl_b32 s14, s1, 10
	s_cmp_eq_u32 s0, 0
	s_cselect_b64 s[24:25], -1, 0
	s_lshl_b32 s2, s2, 8
	s_waitcnt vmcnt(8)
	s_barrier
	s_waitcnt vmcnt(6)
	s_add_i32 s2, s2, 0
	v_or_b32_e32 v0, 0x10000, v0
	s_mul_i32 s64, s10, 0x1800
	s_lshl_b32 s0, s3, 10
	s_mov_b32 s1, s65
	s_mul_i32 s10, s3, 0x1800
	s_mov_b32 s11, s65
	s_lshl_b32 s12, s3, 12
	s_add_i32 s74, s2, s14
	s_lshl_b32 s73, s3, 18
	s_add_i32 s74, s74, 0x21000
	v_add_u32_e32 v245, 0, v0
	v_add_u32_e32 v246, 0, v2
	s_lshl_b64 s[26:27], s[64:65], 2
	s_lshl_b64 s[28:29], s[12:13], 2
	s_lshl_b64 s[30:31], s[0:1], 2
	s_lshl_b64 s[34:35], s[10:11], 2
	v_readlane_b32 s10, v252, 34
	v_readlane_b32 s11, v252, 31
	s_barrier
	s_branch .LBB0_1639
